# speedup vs baseline: 1.0014x; 1.0014x over previous
.LBB2_10:
	s_setprio 1
	s_waitcnt vmcnt(11)
	v_mfma_f32_16x16x32_f16 v[74:77], v[66:69], v[18:21], 0
	s_cmp_lt_u32 s25, 2
	s_cselect_b64 s[14:15], -1, 0
	s_cmp_gt_u32 s25, 1
	s_waitcnt vmcnt(9)
	v_mfma_f32_16x16x32_f16 v[102:105], v[58:61], v[18:21], 0
	s_mov_b64 s[20:21], -1
	v_mfma_f32_16x16x32_f16 v[106:109], v[66:69], v[26:29], 0
	v_mfma_f32_16x16x32_f16 v[110:113], v[58:61], v[26:29], 0
	v_mfma_f32_16x16x32_f16 v[66:69], v[66:69], v[34:37], 0
	v_mfma_f32_16x16x32_f16 v[58:61], v[58:61], v[34:37], 0
	v_mfma_f32_16x16x32_f16 v[74:77], v[70:73], v[22:25], v[74:77]
	s_waitcnt vmcnt(8)
	v_mfma_f32_16x16x32_f16 v[102:105], v[62:65], v[22:25], v[102:105]
	v_mfma_f32_16x16x32_f16 v[106:109], v[70:73], v[30:33], v[106:109]
	s_nop 4
	v_cvt_pk_f16_f32 v77, v76, v77
	v_cvt_pk_f16_f32 v76, v74, v75
	v_cvt_pk_f16_f32 v75, v104, v105
	v_mfma_f32_16x16x32_f16 v[110:113], v[62:65], v[30:33], v[110:113]
	v_cvt_pk_f16_f32 v74, v102, v103
	ds_write2_b64 v87, v[76:77], v[74:75] offset1:4
	v_cvt_pk_f16_f32 v75, v108, v109
	v_mfma_f32_16x16x32_f16 v[66:69], v[70:73], v[38:41], v[66:69]
	v_cvt_pk_f16_f32 v74, v106, v107
	s_nop 2
	v_cvt_pk_f16_f32 v71, v112, v113
	v_cvt_pk_f16_f32 v70, v110, v111
	v_mfma_f32_16x16x32_f16 v[58:61], v[62:65], v[38:41], v[58:61]
	ds_write2_b64 v88, v[74:75], v[70:71] offset1:4
	v_cvt_pk_f16_f32 v69, v68, v69
	v_cvt_pk_f16_f32 v68, v66, v67
	s_nop 4
	v_cvt_pk_f16_f32 v61, v60, v61
	v_cvt_pk_f16_f32 v60, v58, v59
	ds_write2_b64 v89, v[68:69], v[60:61] offset1:4
	s_setprio 0
	s_waitcnt lgkmcnt(0)
	s_barrier
	v_add_u32_e32 v58, 0x10e00, v86
	ds_read_b128 v[58:61], v58
	ds_read_b128 v[62:65], v90
	ds_read_b128 v[66:69], v90 offset:15360
	ds_read_b128 v[70:73], v91
	s_waitcnt lgkmcnt(2)
	v_pk_fma_f16 v77, v58, v62, 0
	v_add_u32_e32 v62, 0x10e10, v86
	v_pk_fma_f16 v74, v61, v65, 0
	v_pk_fma_f16 v75, v60, v64, 0
	v_pk_fma_f16 v76, v59, v63, 0
	ds_read_b128 v[62:65], v62
	s_waitcnt lgkmcnt(2)
	v_pk_fma_f16 v101, v61, v69, 0
	v_pk_fma_f16 v102, v60, v68, 0
	v_pk_fma_f16 v103, v59, v67, 0
	v_pk_fma_f16 v66, v58, v66, 0
	ds_read_b128 v[58:61], v91 offset:15360
	s_waitcnt lgkmcnt(1)
	v_pk_fma_f16 v77, v62, v70, v77
	v_pk_fma_f16 v76, v63, v71, v76
	v_pk_fma_f16 v75, v64, v72, v75
	v_pk_fma_f16 v74, v65, v73, v74
	s_waitcnt lgkmcnt(0)
	v_pk_fma_f16 v104, v62, v58, v66
	v_add_u32_e32 v58, 0x10e20, v86
	ds_read_b128 v[66:69], v58
	ds_read_b128 v[70:73], v92
	v_pk_fma_f16 v103, v63, v59, v103
	v_pk_fma_f16 v102, v64, v60, v102
	v_pk_fma_f16 v101, v65, v61, v101
	ds_read_b128 v[58:61], v92 offset:15360
	v_add_u32_e32 v62, 0x10e30, v86
	s_waitcnt lgkmcnt(1)
	v_pk_fma_f16 v74, v69, v73, v74
	v_pk_fma_f16 v75, v68, v72, v75
	v_pk_fma_f16 v76, v67, v71, v76
	v_pk_fma_f16 v77, v66, v70, v77
	ds_read_b128 v[62:65], v62
	s_waitcnt lgkmcnt(1)
	v_pk_fma_f16 v101, v69, v61, v101
	ds_read_b128 v[70:73], v93
	v_pk_fma_f16 v102, v68, v60, v102
	v_pk_fma_f16 v103, v67, v59, v103
	v_pk_fma_f16 v66, v66, v58, v104
	ds_read_b128 v[58:61], v93 offset:15360
	s_waitcnt lgkmcnt(1)
	v_pk_fma_f16 v77, v62, v70, v77
	v_pk_fma_f16 v76, v63, v71, v76
	v_pk_fma_f16 v75, v64, v72, v75
	v_pk_fma_f16 v74, v65, v73, v74
	s_waitcnt lgkmcnt(0)
	v_pk_fma_f16 v104, v62, v58, v66
	v_add_u32_e32 v58, 0x10e40, v86
	ds_read_b128 v[66:69], v58
	ds_read_b128 v[70:73], v94
	v_pk_fma_f16 v103, v63, v59, v103
	v_pk_fma_f16 v102, v64, v60, v102
	v_pk_fma_f16 v101, v65, v61, v101
	ds_read_b128 v[58:61], v94 offset:15360
	v_add_u32_e32 v62, 0x10e50, v86
	s_waitcnt lgkmcnt(1)
	v_pk_fma_f16 v74, v69, v73, v74
	v_pk_fma_f16 v75, v68, v72, v75
	v_pk_fma_f16 v76, v67, v71, v76
	v_pk_fma_f16 v77, v66, v70, v77
	ds_read_b128 v[62:65], v62
	s_waitcnt lgkmcnt(1)
	v_pk_fma_f16 v101, v69, v61, v101
	ds_read_b128 v[70:73], v95
	v_pk_fma_f16 v102, v68, v60, v102
	v_pk_fma_f16 v103, v67, v59, v103
	v_pk_fma_f16 v66, v66, v58, v104
	ds_read_b128 v[58:61], v95 offset:15360
	s_waitcnt lgkmcnt(1)
	v_pk_fma_f16 v77, v62, v70, v77
	v_pk_fma_f16 v76, v63, v71, v76
	v_pk_fma_f16 v75, v64, v72, v75
	v_pk_fma_f16 v74, v65, v73, v74
	s_waitcnt lgkmcnt(0)
	v_pk_fma_f16 v104, v62, v58, v66
	v_add_u32_e32 v58, 0x10e60, v86
	ds_read_b128 v[66:69], v58
	ds_read_b128 v[70:73], v96
	v_pk_fma_f16 v103, v63, v59, v103
	v_pk_fma_f16 v102, v64, v60, v102
	v_pk_fma_f16 v101, v65, v61, v101
	ds_read_b128 v[58:61], v96 offset:15360
	v_add_u32_e32 v62, 0x10e70, v86
	s_waitcnt lgkmcnt(1)
	v_pk_fma_f16 v74, v69, v73, v74
	v_pk_fma_f16 v75, v68, v72, v75
	v_pk_fma_f16 v76, v67, v71, v76
	v_pk_fma_f16 v77, v66, v70, v77
	ds_read_b128 v[62:65], v62
	s_waitcnt lgkmcnt(1)
	v_pk_fma_f16 v101, v69, v61, v101
	ds_read_b128 v[70:73], v97
	v_pk_fma_f16 v102, v68, v60, v102
	v_pk_fma_f16 v103, v67, v59, v103
	v_pk_fma_f16 v66, v66, v58, v104
	ds_read_b128 v[58:61], v97 offset:15360
	s_waitcnt lgkmcnt(1)
	v_pk_fma_f16 v77, v62, v70, v77
	v_pk_fma_f16 v76, v63, v71, v76
	v_pk_fma_f16 v75, v64, v72, v75
	v_pk_fma_f16 v74, v65, v73, v74
	s_waitcnt lgkmcnt(0)
	v_pk_fma_f16 v104, v62, v58, v66
	v_add_u32_e32 v58, 0x10e80, v86
	ds_read_b128 v[66:69], v58
	ds_read_b128 v[70:73], v98
	v_pk_fma_f16 v103, v63, v59, v103
	v_pk_fma_f16 v102, v64, v60, v102
	v_pk_fma_f16 v101, v65, v61, v101
	ds_read_b128 v[62:65], v98 offset:15360
	s_waitcnt lgkmcnt(1)
	v_pk_fma_f16 v61, v69, v73, v74
	v_pk_fma_f16 v60, v68, v72, v75
	v_pk_fma_f16 v59, v67, v71, v76
	v_pk_fma_f16 v58, v66, v70, v77
	s_waitcnt lgkmcnt(0)
	v_pk_fma_f16 v65, v69, v65, v101
	v_pk_fma_f16 v64, v68, v64, v102
	v_pk_fma_f16 v63, v67, v63, v103
	v_pk_fma_f16 v62, v66, v62, v104
	s_cbranch_scc0 .LBB2_12
	global_store_dwordx4 v[82:83], v[58:61], off sc1
	global_store_dwordx4 v[80:81], v[62:65], off sc1
	s_mov_b64 s[20:21], 0
